# v63 + work-queue tail split from entry 40: entries 40..63 keep half of their weight-copy chunk, 24 extra copy-only entries per XCD (88 entries)
# speedup vs baseline: 1.0050x; 1.0050x over previous
.LBB6_896:
	s_or_b64 exec, exec, s[2:3]
	v_readlane_b32 s0, v254, 30
	s_waitcnt lgkmcnt(0)
	s_barrier
	v_mov_b32_e32 v2, s0
	ds_read_b32 v2, v2
	s_mov_b64 s[2:3], -1
	s_waitcnt lgkmcnt(0)
	s_barrier
	v_readfirstlane_b32 s0, v2
	s_cmp_gt_i32 s0, 0x57
	s_cbranch_scc1 .LBB6_891
	s_cmp_gt_i32 s0, 47
	s_cbranch_scc0 .LBB6_899
	s_sub_i32 s1, s0, 48
	s_lshr_b32 s92, s1, 1
	s_mov_b64 s[2:3], 0

.LBB6_901:
	s_lshl_b32 s84, s0, 3
	s_or_b32 s1, s84, s59
	s_lshl_b32 s2, s1, 1
	s_add_i32 s3, s1, 0x140
	s_cmp_lt_u32 s1, 0x140
	s_cselect_b32 s2, s2, s3
	s_mul_i32 s2, s63, s2
	s_lshr_b32 s2, s2, 10
	s_and_b32 s90, s2, 0xffffffe0
	s_add_i32 s1, s1, 1
	s_lshl_b32 s2, s1, 1
	s_add_i32 s3, s1, 0x140
	s_cmp_lt_u32 s1, 0x140
	s_cselect_b32 s2, s2, s3
	s_mul_i32 s2, s63, s2
	s_lshr_b32 s2, s2, 10
	s_and_b32 s91, s2, 0xffffffe0
	s_bitcmp0_b32 s0, 0
	s_cselect_b64 s[22:23], -1, 0
	s_and_b64 vcc, exec, s[22:23]
	s_cbranch_vccnz .LBB6_1210
	v_readfirstlane_b32 s98, v0
	s_nop 0
	s_bitcmp1_b32 s98, 8
	s_cbranch_scc0 .Ldephase_a
	s_sleep 80
